# prefetch in-proj weights (25MB) into MALL/L2 at phase B start, blocking
# speedup vs baseline: 1.0071x; 1.0071x over previous
.LBB0_3295:
	v_readlane_b32 s2, v254, 0
	v_readlane_b32 s3, v254, 1
	s_load_dword s0, s[2:3], 0x128
	s_mul_i32 s4, s48, 13
	s_mov_b32 s49, s93
	s_add_i32 s69, s4, 2
	v_writelane_b32 v254, s48, 51
	s_waitcnt lgkmcnt(0)
	s_cmp_le_i32 s0, s69
	v_writelane_b32 v254, s49, 52
	s_cbranch_scc0 .LBB0_3540
	s_load_dword s0, s[2:3], 0x12c
	s_waitcnt lgkmcnt(0)
	s_cmp_ge_i32 s69, s0
	s_cbranch_scc1 .LBB0_3540
	v_readlane_b32 s2, v254, 0
	v_readlane_b32 s3, v254, 1
	s_load_dwordx2 s[6:7], s[2:3], 0x120
	v_lshlrev_b32_e32 v0, 4, v235
	s_mul_i32 s12, s48, 0x1400000
	s_mul_i32 s13, s43, 0x14000
	s_add_u32 s12, s12, s13
	s_add_u32 s12, s12, 0x1100000
	s_lshl_b32 s13, s48, 22
	s_lshl_b32 s14, s43, 14
	s_add_u32 s13, s13, s14
	s_add_u32 s13, s13, 0x100000
	s_waitcnt lgkmcnt(0)
	s_add_u32 s8, s6, s12
	s_addc_u32 s9, s7, 0
	s_add_u32 s12, s6, s13
	s_addc_u32 s13, s7, 0
	global_load_dwordx4 v[4:7], v0, s[8:9]
	v_mov_b32_e32 v3, v0
	v_add_u32_e32 v3, 0x2000, v3
	global_load_dwordx4 v[8:11], v3, s[8:9]
	v_add_u32_e32 v3, 0x2000, v3
	global_load_dwordx4 v[12:15], v3, s[8:9]
	v_add_u32_e32 v3, 0x2000, v3
	global_load_dwordx4 v[16:19], v3, s[8:9]
	v_add_u32_e32 v3, 0x2000, v3
	global_load_dwordx4 v[20:23], v3, s[8:9]
	v_add_u32_e32 v3, 0x2000, v3
	global_load_dwordx4 v[24:27], v3, s[8:9]
	v_add_u32_e32 v3, 0x2000, v3
	global_load_dwordx4 v[28:31], v3, s[8:9]
	v_add_u32_e32 v3, 0x2000, v3
	global_load_dwordx4 v[32:35], v3, s[8:9]
	v_add_u32_e32 v3, 0x2000, v3
	global_load_dwordx4 v[36:39], v3, s[8:9]
	v_add_u32_e32 v3, 0x2000, v3
	global_load_dwordx4 v[40:43], v3, s[8:9]
	global_load_dwordx4 v[44:47], v0, s[12:13]
	v_add_u32_e32 v3, 0x2000, v0
	global_load_dwordx4 v[48:51], v3, s[12:13]
	s_waitcnt vmcnt(0)
	s_mov_b32 s70, s43
	v_mov_b32_e32 v0, v235
	v_readlane_b32 s0, v254, 6
	s_cmpk_lt_i32 s70, 0x100
	s_nop 0
	v_lshl_add_u32 v242, s0, 6, v218
	v_mov_b32_e32 v6, v242
	s_cselect_b64 s[6:7], -1, 0
	s_cmpk_gt_i32 s70, 0xff
	v_readfirstlane_b32 s0, v6
	s_cbranch_scc1 .LBB0_3303
	s_ashr_i32 s4, s70, 31
	s_lshr_b32 s4, s4, 29
	s_add_i32 s8, s70, s4
	s_and_b32 s4, s8, -8
	s_sub_i32 s9, s70, s4
	s_cmp_gt_i32 s9, -1
	s_mov_b64 s[4:5], -1
	s_cbranch_scc0 .LBB0_3300
	s_lshl_b32 s10, s9, 5
	s_mov_b64 s[4:5], 0
